# adds GEMM epilogue output stores sc1 (write-through) so the seam release fence has less dirty L2 to write back
# baseline (speedup 1.0000x reference)
.LBB0_194:
	v_lshl_add_u32 v152, s85, 8, v1
	s_lshl_b32 s40, s14, 8
	s_cmp_lt_i32 s14, 58
	s_mov_b64 s[42:43], -1
	v_or_b32_e32 v150, 16, v152
	v_or_b32_e32 v148, 32, v152
	v_or_b32_e32 v146, 48, v152
	s_cbranch_scc0 .LBB0_196
	s_ashr_i32 s41, s40, 31
	v_lshl_add_u64 v[160:161], s[40:41], 1, v[138:139]
	s_movk_i32 s9, 0x7400
	v_mad_i64_i32 v[162:163], s[42:43], v152, s9, v[160:161]
	v_cvt_pk_bf16_f32 v156, v128, v129
	v_cvt_pk_bf16_f32 v157, v130, v131
	v_cvt_pk_bf16_f32 v158, v124, v125
	v_cvt_pk_bf16_f32 v159, v126, v127
	global_store_dwordx4 v[162:163], v[156:159], off sc1
	v_add_u32_e32 v147, 0x80, v152
	s_nop 0
	v_cvt_pk_bf16_f32 v156, v108, v109
	v_cvt_pk_bf16_f32 v157, v110, v111
	v_cvt_pk_bf16_f32 v158, v100, v101
	v_cvt_pk_bf16_f32 v159, v102, v103
	global_store_dwordx4 v[162:163], v[156:159], off offset:256 sc1
	v_mad_i64_i32 v[162:163], s[42:43], v150, s9, v[160:161]
	s_nop 0
	v_cvt_pk_bf16_f32 v156, v120, v121
	v_cvt_pk_bf16_f32 v157, v122, v123
	v_cvt_pk_bf16_f32 v158, v116, v117
	v_cvt_pk_bf16_f32 v159, v118, v119
	global_store_dwordx4 v[162:163], v[156:159], off sc1
	s_nop 1
	v_cvt_pk_bf16_f32 v156, v92, v93
	v_cvt_pk_bf16_f32 v157, v94, v95
	v_cvt_pk_bf16_f32 v158, v84, v85
	v_cvt_pk_bf16_f32 v159, v86, v87
	global_store_dwordx4 v[162:163], v[156:159], off offset:256 sc1
	v_mad_i64_i32 v[162:163], s[42:43], v148, s9, v[160:161]
	s_nop 0
	v_cvt_pk_bf16_f32 v156, v112, v113
	v_cvt_pk_bf16_f32 v157, v114, v115
	v_cvt_pk_bf16_f32 v158, v104, v105
	v_cvt_pk_bf16_f32 v159, v106, v107
	global_store_dwordx4 v[162:163], v[156:159], off sc1
	s_nop 1
	v_cvt_pk_bf16_f32 v156, v80, v81
	v_cvt_pk_bf16_f32 v157, v82, v83
	v_cvt_pk_bf16_f32 v158, v76, v77
	v_cvt_pk_bf16_f32 v159, v78, v79
	global_store_dwordx4 v[162:163], v[156:159], off offset:256 sc1
	v_mad_i64_i32 v[162:163], s[42:43], v146, s9, v[160:161]
	s_nop 0
	v_cvt_pk_bf16_f32 v156, v96, v97
	v_cvt_pk_bf16_f32 v157, v98, v99
	v_cvt_pk_bf16_f32 v158, v88, v89
	v_cvt_pk_bf16_f32 v159, v90, v91
	global_store_dwordx4 v[162:163], v[156:159], off sc1
	s_nop 1
	v_cvt_pk_bf16_f32 v156, v72, v73
	v_cvt_pk_bf16_f32 v157, v74, v75
	v_cvt_pk_bf16_f32 v158, v68, v69
	v_cvt_pk_bf16_f32 v159, v70, v71
	global_store_dwordx4 v[162:163], v[156:159], off offset:256 sc1
	v_mad_i64_i32 v[162:163], s[42:43], v147, s9, v[160:161]
	s_nop 0
	v_cvt_pk_bf16_f32 v156, v64, v65
	v_cvt_pk_bf16_f32 v157, v66, v67
	v_cvt_pk_bf16_f32 v158, v60, v61
	v_cvt_pk_bf16_f32 v159, v62, v63
	global_store_dwordx4 v[162:163], v[156:159], off sc1
	v_add_u32_e32 v147, 0x90, v152
	s_nop 0
	v_cvt_pk_bf16_f32 v156, v48, v49
	v_cvt_pk_bf16_f32 v157, v50, v51
	v_cvt_pk_bf16_f32 v158, v44, v45
	v_cvt_pk_bf16_f32 v159, v46, v47
	global_store_dwordx4 v[162:163], v[156:159], off offset:256 sc1
	v_mad_i64_i32 v[162:163], s[42:43], v147, s9, v[160:161]
	s_nop 0
	v_cvt_pk_bf16_f32 v156, v56, v57
	v_cvt_pk_bf16_f32 v157, v58, v59
	v_cvt_pk_bf16_f32 v158, v52, v53
	v_cvt_pk_bf16_f32 v159, v54, v55
	global_store_dwordx4 v[162:163], v[156:159], off sc1
	v_add_u32_e32 v147, 0xa0, v152
	s_nop 0
	v_cvt_pk_bf16_f32 v156, v32, v33
	v_cvt_pk_bf16_f32 v157, v34, v35
	v_cvt_pk_bf16_f32 v158, v28, v29
	v_cvt_pk_bf16_f32 v159, v30, v31
	global_store_dwordx4 v[162:163], v[156:159], off offset:256 sc1
	v_mad_i64_i32 v[162:163], s[42:43], v147, s9, v[160:161]
	s_nop 0
	v_cvt_pk_bf16_f32 v156, v40, v41
	v_cvt_pk_bf16_f32 v157, v42, v43
	v_cvt_pk_bf16_f32 v158, v36, v37
	v_cvt_pk_bf16_f32 v159, v38, v39
	global_store_dwordx4 v[162:163], v[156:159], off sc1
	v_add_u32_e32 v147, 0xb0, v152
	v_mad_i64_i32 v[160:161], s[42:43], v147, s9, v[160:161]
	v_cvt_pk_bf16_f32 v156, v16, v17
	v_cvt_pk_bf16_f32 v157, v18, v19
	v_cvt_pk_bf16_f32 v158, v12, v13
	v_cvt_pk_bf16_f32 v159, v14, v15
	global_store_dwordx4 v[162:163], v[156:159], off offset:256 sc1
	s_mov_b64 s[42:43], 0
	s_nop 0
	v_cvt_pk_bf16_f32 v156, v24, v25
	v_cvt_pk_bf16_f32 v157, v26, v27
	v_cvt_pk_bf16_f32 v158, v20, v21
	v_cvt_pk_bf16_f32 v159, v22, v23
	global_store_dwordx4 v[160:161], v[156:159], off sc1
	s_nop 1
	v_cvt_pk_bf16_f32 v156, v8, v9
	v_cvt_pk_bf16_f32 v157, v10, v11
	v_cvt_pk_bf16_f32 v158, v4, v5
	v_cvt_pk_bf16_f32 v159, v6, v7
	global_store_dwordx4 v[160:161], v[156:159], off offset:256 sc1

.LBB0_664:
	s_ashr_i32 s40, s84, 3
	s_ashr_i32 s41, s40, 31
	s_lshl_b64 s[40:41], s[40:41], 26
	s_add_u32 s11, s68, s40
	s_addc_u32 s13, s69, s41
	s_lshl_b32 s40, s84, 9
	s_and_b32 s40, s40, 0xe00
	v_lshl_add_u32 v146, s85, 8, v1
	s_add_u32 s40, s11, s40
	s_addc_u32 s41, s13, 0
	v_ashrrev_i32_e32 v147, 31, v146
	v_lshl_add_u64 v[148:149], s[40:41], 0, v[2:3]
	v_lshlrev_b64 v[150:151], 12, v[146:147]
	v_lshl_add_u64 v[150:151], v[148:149], 0, v[150:151]
	s_mov_b32 s11, 0x80000
	s_mov_b64 s[40:41], 0x80000
	v_cvt_pk_bf16_f32 v64, v64, v65
	v_cvt_pk_bf16_f32 v65, v66, v67
	v_cvt_pk_bf16_f32 v66, v60, v61
	v_add_co_u32_e32 v60, vcc, s11, v150
	v_cvt_pk_bf16_f32 v72, v72, v73
	v_cvt_pk_bf16_f32 v73, v74, v75
	v_cvt_pk_bf16_f32 v74, v68, v69
	v_lshl_add_u64 v[68:69], v[150:151], 0, s[40:41]
	v_addc_co_u32_e32 v61, vcc, 0, v151, vcc
	v_cvt_pk_bf16_f32 v48, v48, v49
	v_cvt_pk_bf16_f32 v49, v50, v51
	v_cvt_pk_bf16_f32 v50, v44, v45
	v_cvt_pk_bf16_f32 v51, v46, v47
	s_mov_b32 s11, 0x90000
	global_store_dwordx4 v[68:69], v[48:51], off offset:256 sc1
	s_mov_b64 s[40:41], 0x90000
	v_cvt_pk_bf16_f32 v112, v112, v113
	v_add_co_u32_e32 v50, vcc, s11, v150
	v_cvt_pk_bf16_f32 v113, v114, v115
	v_cvt_pk_bf16_f32 v114, v108, v109
	v_or_b32_e32 v108, 16, v146
	v_lshl_add_u64 v[48:49], v[150:151], 0, s[40:41]
	v_addc_co_u32_e32 v51, vcc, 0, v151, vcc
	v_cvt_pk_bf16_f32 v32, v32, v33
	v_cvt_pk_bf16_f32 v33, v34, v35
	v_cvt_pk_bf16_f32 v34, v28, v29
	v_cvt_pk_bf16_f32 v35, v30, v31
	s_mov_b32 s11, 0xa0000
	v_ashrrev_i32_e32 v109, 31, v108
	v_cvt_pk_bf16_f32 v96, v96, v97
	v_cvt_pk_bf16_f32 v97, v98, v99
	v_cvt_pk_bf16_f32 v98, v92, v93
	v_or_b32_e32 v92, 32, v146
	global_store_dwordx4 v[48:49], v[32:35], off offset:256 sc1
	s_mov_b64 s[40:41], 0xa0000
	v_cvt_pk_bf16_f32 v115, v110, v111
	v_add_co_u32_e32 v34, vcc, s11, v150
	v_lshlrev_b64 v[108:109], 12, v[108:109]
	v_ashrrev_i32_e32 v93, 31, v92
	v_cvt_pk_bf16_f32 v80, v80, v81
	v_cvt_pk_bf16_f32 v81, v82, v83
	v_cvt_pk_bf16_f32 v82, v76, v77
	v_or_b32_e32 v76, 48, v146
	v_lshl_add_u64 v[32:33], v[150:151], 0, s[40:41]
	v_addc_co_u32_e32 v35, vcc, 0, v151, vcc
	v_cvt_pk_bf16_f32 v16, v16, v17
	v_cvt_pk_bf16_f32 v17, v18, v19
	v_cvt_pk_bf16_f32 v18, v12, v13
	v_cvt_pk_bf16_f32 v19, v14, v15
	s_mov_b32 s11, 0xb0000
	global_store_dwordx4 v[150:151], v[112:115], off offset:256 sc1
	v_cvt_pk_bf16_f32 v99, v94, v95
	v_lshlrev_b64 v[92:93], 12, v[92:93]
	v_lshl_add_u64 v[112:113], v[148:149], 0, v[108:109]
	v_ashrrev_i32_e32 v77, 31, v76
	global_store_dwordx4 v[32:33], v[16:19], off offset:256 sc1
	global_store_dwordx4 v[112:113], v[96:99], off offset:256 sc1
	v_cvt_pk_bf16_f32 v83, v78, v79
	v_add_co_u32_e32 v18, vcc, s11, v150
	v_lshl_add_u64 v[96:97], v[148:149], 0, v[92:93]
	v_lshlrev_b64 v[76:77], 12, v[76:77]
	s_mov_b64 s[40:41], 0xb0000
	v_addc_co_u32_e32 v19, vcc, 0, v151, vcc
	v_readlane_b32 s88, v239, 24
	v_cvt_pk_bf16_f32 v128, v128, v129
	v_cvt_pk_bf16_f32 v129, v130, v131
	v_cvt_pk_bf16_f32 v130, v124, v125
	v_cvt_pk_bf16_f32 v131, v126, v127
	v_cvt_pk_bf16_f32 v108, v120, v121
	v_cvt_pk_bf16_f32 v109, v122, v123
	v_cvt_pk_bf16_f32 v110, v116, v117
	v_cvt_pk_bf16_f32 v111, v118, v119
	v_cvt_pk_bf16_f32 v92, v104, v105
	v_cvt_pk_bf16_f32 v93, v106, v107
	v_cvt_pk_bf16_f32 v94, v100, v101
	v_cvt_pk_bf16_f32 v95, v102, v103
	global_store_dwordx4 v[96:97], v[80:83], off offset:256 sc1
	v_cvt_pk_bf16_f32 v78, v84, v85
	v_cvt_pk_bf16_f32 v79, v86, v87
	v_lshl_add_u64 v[80:81], v[148:149], 0, v[76:77]
	v_cvt_pk_bf16_f32 v76, v88, v89
	v_cvt_pk_bf16_f32 v77, v90, v91
	v_cvt_pk_bf16_f32 v75, v70, v71
	v_cvt_pk_bf16_f32 v67, v62, v63
	v_cvt_pk_bf16_f32 v44, v56, v57
	v_cvt_pk_bf16_f32 v45, v58, v59
	v_cvt_pk_bf16_f32 v46, v52, v53
	v_cvt_pk_bf16_f32 v47, v54, v55
	v_cvt_pk_bf16_f32 v28, v40, v41
	v_cvt_pk_bf16_f32 v29, v42, v43
	v_cvt_pk_bf16_f32 v30, v36, v37
	v_cvt_pk_bf16_f32 v31, v38, v39
	v_lshl_add_u64 v[16:17], v[150:151], 0, s[40:41]
	v_cvt_pk_bf16_f32 v12, v24, v25
	v_cvt_pk_bf16_f32 v13, v26, v27
	v_cvt_pk_bf16_f32 v14, v20, v21
	v_cvt_pk_bf16_f32 v15, v22, v23
	v_cvt_pk_bf16_f32 v8, v8, v9
	v_cvt_pk_bf16_f32 v9, v10, v11
	v_cvt_pk_bf16_f32 v10, v4, v5
	v_cvt_pk_bf16_f32 v11, v6, v7
	s_and_b64 vcc, exec, s[4:5]
	s_mov_b64 s[4:5], -1
	v_readlane_b32 s89, v239, 25
	v_readlane_b32 s90, v239, 26
	v_readlane_b32 s91, v239, 27
	global_store_dwordx4 v[150:151], v[128:131], off sc1
	global_store_dwordx4 v[112:113], v[108:111], off sc1
	global_store_dwordx4 v[96:97], v[92:95], off sc1
	global_store_dwordx4 v[80:81], v[76:79], off sc1
	global_store_dwordx4 v[80:81], v[72:75], off offset:256 sc1
	global_store_dwordx4 v[60:61], v[64:67], off sc1
	global_store_dwordx4 v[50:51], v[44:47], off sc1
	global_store_dwordx4 v[34:35], v[28:31], off sc1
	global_store_dwordx4 v[18:19], v[12:15], off sc1
	global_store_dwordx4 v[16:17], v[8:11], off offset:256 sc1
	s_cbranch_vccnz .LBB0_651
	s_andn2_b64 vcc, exec, s[6:7]
	s_cbranch_vccnz .LBB0_650
	s_barrier
	s_branch .LBB0_650

.LBB0_735:
	v_lshl_or_b32 v152, s82, 6, v217
	v_lshl_add_u32 v153, s83, 19, v218
	v_add_u32_e32 v2, v153, v152
	v_lshlrev_b64 v[198:199], 1, v[2:3]
	v_add_u32_e32 v154, 0x2000000, v153
	v_add_u32_e32 v155, 0x4000000, v153
	v_add_u32_e32 v156, 0x6000000, v153
	v_lshl_add_u64 v[144:145], s[68:69], 0, v[198:199]
	v_add_u32_e32 v146, v154, v152
	v_mov_b32_e32 v147, v3
	v_add_u32_e32 v148, v155, v152
	v_mov_b32_e32 v149, v3
	v_add_u32_e32 v150, v156, v152
	v_mov_b32_e32 v151, v3
	v_lshl_add_u64 v[146:147], v[146:147], 1, s[68:69]
	v_lshl_add_u64 v[148:149], v[148:149], 1, s[68:69]
	v_lshl_add_u64 v[150:151], v[150:151], 1, s[68:69]
	global_load_dwordx2 v[206:207], v[144:145], off
	global_load_dwordx2 v[204:205], v[146:147], off
	global_load_dwordx2 v[202:203], v[148:149], off
	global_load_dwordx2 v[200:201], v[150:151], off
	v_add_u32_e32 v157, 0x8000, v152
	v_add_u32_e32 v144, v157, v153
	v_mov_b32_e32 v145, v3
	v_lshl_add_u64 v[144:145], v[144:145], 1, s[68:69]
	v_add_u32_e32 v146, v154, v157
	v_mov_b32_e32 v147, v3
	v_add_u32_e32 v148, v155, v157
	v_mov_b32_e32 v149, v3
	v_add_u32_e32 v150, v156, v157
	v_mov_b32_e32 v151, v3
	v_lshl_add_u64 v[146:147], v[146:147], 1, s[68:69]
	v_lshl_add_u64 v[148:149], v[148:149], 1, s[68:69]
	v_lshl_add_u64 v[150:151], v[150:151], 1, s[68:69]
	global_load_dwordx2 v[196:197], v[144:145], off
	global_load_dwordx2 v[194:195], v[146:147], off
	global_load_dwordx2 v[192:193], v[148:149], off
	global_load_dwordx2 v[190:191], v[150:151], off
	v_add_u32_e32 v220, 0x10000, v152
	v_add_u32_e32 v144, v220, v153
	v_mov_b32_e32 v145, v3
	v_lshl_add_u64 v[144:145], v[144:145], 1, s[68:69]
	v_add_u32_e32 v146, v154, v220
	v_mov_b32_e32 v147, v3
	v_add_u32_e32 v148, v155, v220
	v_mov_b32_e32 v149, v3
	v_add_u32_e32 v150, v156, v220
	v_mov_b32_e32 v151, v3
	v_lshl_add_u64 v[146:147], v[146:147], 1, s[68:69]
	v_lshl_add_u64 v[148:149], v[148:149], 1, s[68:69]
	v_lshl_add_u64 v[150:151], v[150:151], 1, s[68:69]
	global_load_dwordx2 v[188:189], v[144:145], off
	global_load_dwordx2 v[186:187], v[146:147], off
	global_load_dwordx2 v[184:185], v[148:149], off
	global_load_dwordx2 v[182:183], v[150:151], off
	v_add_u32_e32 v222, 0x18000, v152
	v_add_u32_e32 v144, v222, v153
	v_mov_b32_e32 v145, v3
	v_lshl_add_u64 v[144:145], v[144:145], 1, s[68:69]
	v_add_u32_e32 v146, v154, v222
	v_mov_b32_e32 v147, v3
	v_add_u32_e32 v148, v155, v222
	v_mov_b32_e32 v149, v3
	v_add_u32_e32 v150, v156, v222
	v_mov_b32_e32 v151, v3
	v_lshl_add_u64 v[146:147], v[146:147], 1, s[68:69]
	v_lshl_add_u64 v[148:149], v[148:149], 1, s[68:69]
	v_lshl_add_u64 v[150:151], v[150:151], 1, s[68:69]
	global_load_dwordx2 v[180:181], v[144:145], off
	global_load_dwordx2 v[178:179], v[146:147], off
	global_load_dwordx2 v[176:177], v[148:149], off
	global_load_dwordx2 v[174:175], v[150:151], off
	v_add_u32_e32 v221, 0x40000, v153
	v_add_u32_e32 v144, v221, v152
	v_mov_b32_e32 v145, v3
	v_add_u32_e32 v223, 0x2040000, v153
	v_add_u32_e32 v224, 0x4040000, v153
	v_add_u32_e32 v225, 0x6040000, v153
	v_lshl_add_u64 v[144:145], v[144:145], 1, s[68:69]
	v_add_u32_e32 v146, v223, v152
	v_mov_b32_e32 v147, v3
	v_add_u32_e32 v148, v224, v152
	v_mov_b32_e32 v149, v3
	v_add_u32_e32 v150, v225, v152
	v_mov_b32_e32 v151, v3
	v_lshl_add_u64 v[146:147], v[146:147], 1, s[68:69]
	v_lshl_add_u64 v[148:149], v[148:149], 1, s[68:69]
	v_lshl_add_u64 v[150:151], v[150:151], 1, s[68:69]
	global_load_dwordx2 v[172:173], v[144:145], off
	global_load_dwordx2 v[170:171], v[146:147], off
	global_load_dwordx2 v[168:169], v[148:149], off
	global_load_dwordx2 v[166:167], v[150:151], off
	v_add_u32_e32 v144, v221, v157
	v_mov_b32_e32 v145, v3
	v_lshl_add_u64 v[144:145], v[144:145], 1, s[68:69]
	v_add_u32_e32 v146, v223, v157
	v_mov_b32_e32 v147, v3
	v_add_u32_e32 v148, v224, v157
	v_mov_b32_e32 v149, v3
	v_add_u32_e32 v150, v225, v157
	v_mov_b32_e32 v151, v3
	v_lshl_add_u64 v[146:147], v[146:147], 1, s[68:69]
	v_lshl_add_u64 v[148:149], v[148:149], 1, s[68:69]
	v_lshl_add_u64 v[150:151], v[150:151], 1, s[68:69]
	global_load_dwordx2 v[164:165], v[144:145], off
	global_load_dwordx2 v[162:163], v[146:147], off
	global_load_dwordx2 v[160:161], v[148:149], off
	global_load_dwordx2 v[158:159], v[150:151], off
	v_add_u32_e32 v144, v221, v220
	v_mov_b32_e32 v145, v3
	v_add_u32_e32 v148, v224, v220
	v_mov_b32_e32 v149, v3
	v_add_u32_e32 v150, v225, v220
	v_mov_b32_e32 v151, v3
	v_lshl_add_u64 v[144:145], v[144:145], 1, s[68:69]
	v_add_u32_e32 v146, v223, v220
	v_mov_b32_e32 v147, v3
	v_lshl_add_u64 v[148:149], v[148:149], 1, s[68:69]
	v_lshl_add_u64 v[150:151], v[150:151], 1, s[68:69]
	v_mul_f32_e32 v128, 0xbfb8aa3b, v128
	v_lshl_add_u64 v[146:147], v[146:147], 1, s[68:69]
	global_load_dwordx2 v[156:157], v[144:145], off
	global_load_dwordx2 v[154:155], v[146:147], off
	global_load_dwordx2 v[152:153], v[148:149], off
	s_nop 0
	global_load_dwordx2 v[150:151], v[150:151], off
	v_add_u32_e32 v148, v224, v222
	v_mov_b32_e32 v149, v3
	v_exp_f32_e32 v224, v128
	v_mul_f32_e32 v128, 0xbfb8aa3b, v129
	v_add_u32_e32 v144, v221, v222
	v_lshl_add_u64 v[220:221], v[148:149], 1, s[68:69]
	v_add_u32_e32 v148, v225, v222
	v_exp_f32_e32 v225, v128
	v_mul_f32_e32 v124, 0xbfb8aa3b, v124
	v_mul_f32_e32 v125, 0xbfb8aa3b, v125
	v_exp_f32_e32 v124, v124
	v_exp_f32_e32 v125, v125
	v_mul_f32_e32 v120, 0xbfb8aa3b, v120
	v_mul_f32_e32 v121, 0xbfb8aa3b, v121
	v_mov_b32_e32 v145, v3
	v_add_u32_e32 v146, v223, v222
	v_mov_b32_e32 v147, v3
	v_exp_f32_e32 v120, v120
	v_exp_f32_e32 v121, v121
	v_mul_f32_e32 v116, 0xbfb8aa3b, v116
	v_mul_f32_e32 v117, 0xbfb8aa3b, v117
	v_lshl_add_u64 v[144:145], v[144:145], 1, s[68:69]
	v_lshl_add_u64 v[146:147], v[146:147], 1, s[68:69]
	v_mul_f32_e32 v130, 0xbfb8aa3b, v130
	v_mul_f32_e32 v131, 0xbfb8aa3b, v131
	v_exp_f32_e32 v116, v116
	v_exp_f32_e32 v117, v117
	v_lshl_add_u64 v[222:223], v[148:149], 1, s[68:69]
	global_load_dwordx2 v[148:149], v[144:145], off
	s_nop 0
	global_load_dwordx2 v[146:147], v[146:147], off
	s_nop 0
	global_load_dwordx2 v[144:145], v[220:221], off
	global_load_dwordx2 v[128:129], v[222:223], off
	v_add_f32_e32 v220, 1.0, v224
	v_add_f32_e32 v221, 1.0, v225
	v_exp_f32_e32 v130, v130
	v_exp_f32_e32 v131, v131
	v_mul_f32_e32 v126, 0xbfb8aa3b, v126
	v_mul_f32_e32 v127, 0xbfb8aa3b, v127
	v_rcp_f32_e32 v220, v220
	v_rcp_f32_e32 v221, v221
	v_add_f32_e32 v124, 1.0, v124
	v_add_f32_e32 v125, 1.0, v125
	v_exp_f32_e32 v126, v126
	v_exp_f32_e32 v127, v127
	v_mul_f32_e32 v122, 0xbfb8aa3b, v122
	v_mul_f32_e32 v123, 0xbfb8aa3b, v123
	v_rcp_f32_e32 v124, v124
	v_rcp_f32_e32 v125, v125
	v_add_f32_e32 v120, 1.0, v120
	v_add_f32_e32 v121, 1.0, v121
	v_exp_f32_e32 v122, v122
	v_exp_f32_e32 v123, v123
	v_mul_f32_e32 v118, 0xbfb8aa3b, v118
	v_mul_f32_e32 v119, 0xbfb8aa3b, v119
	v_rcp_f32_e32 v120, v120
	v_rcp_f32_e32 v121, v121
	v_add_f32_e32 v116, 1.0, v116
	v_add_f32_e32 v117, 1.0, v117
	v_exp_f32_e32 v118, v118
	v_exp_f32_e32 v119, v119
	v_add_f32_e32 v130, 1.0, v130
	v_add_f32_e32 v131, 1.0, v131
	v_rcp_f32_e32 v116, v116
	v_rcp_f32_e32 v117, v117
	s_waitcnt vmcnt(0)
	v_lshlrev_b32_e32 v222, 16, v206
	v_and_b32_e32 v223, 0xffff0000, v206
	v_rcp_f32_e32 v130, v130
	v_rcp_f32_e32 v131, v131
	v_add_f32_e32 v126, 1.0, v126
	v_add_f32_e32 v127, 1.0, v127
	v_pk_fma_f32 v[220:221], v[220:221], v[222:223], 0 op_sel_hi:[1,1,0]
	v_lshlrev_b32_e32 v222, 16, v204
	v_and_b32_e32 v223, 0xffff0000, v204
	v_mul_f32_e32 v112, 0xbfb8aa3b, v112
	v_mul_f32_e32 v113, 0xbfb8aa3b, v113
	v_rcp_f32_e32 v126, v126
	v_rcp_f32_e32 v127, v127
	v_add_f32_e32 v122, 1.0, v122
	v_add_f32_e32 v123, 1.0, v123
	v_pk_fma_f32 v[124:125], v[124:125], v[222:223], v[220:221]
	v_lshlrev_b32_e32 v220, 16, v202
	v_and_b32_e32 v221, 0xffff0000, v202
	v_exp_f32_e32 v112, v112
	v_exp_f32_e32 v113, v113
	v_mul_f32_e32 v108, 0xbfb8aa3b, v108
	v_mul_f32_e32 v109, 0xbfb8aa3b, v109
	v_rcp_f32_e32 v122, v122
	v_rcp_f32_e32 v123, v123
	v_pk_fma_f32 v[120:121], v[120:121], v[220:221], v[124:125]
	v_lshlrev_b32_e32 v124, 16, v200
	v_and_b32_e32 v125, 0xffff0000, v200
	v_add_f32_e32 v118, 1.0, v118
	v_add_f32_e32 v119, 1.0, v119
	v_exp_f32_e32 v108, v108
	v_exp_f32_e32 v109, v109
	v_mul_f32_e32 v104, 0xbfb8aa3b, v104
	v_mul_f32_e32 v105, 0xbfb8aa3b, v105
	v_pk_fma_f32 v[116:117], v[116:117], v[124:125], v[120:121]
	v_rcp_f32_e32 v118, v118
	v_rcp_f32_e32 v119, v119
	v_lshlrev_b32_e32 v120, 16, v207
	v_and_b32_e32 v121, 0xffff0000, v207
	v_exp_f32_e32 v104, v104
	v_exp_f32_e32 v105, v105
	v_mul_f32_e32 v100, 0xbfb8aa3b, v100
	v_mul_f32_e32 v101, 0xbfb8aa3b, v101
	v_pk_fma_f32 v[120:121], v[130:131], v[120:121], 0 op_sel_hi:[1,1,0]
	v_lshlrev_b32_e32 v124, 16, v205
	v_and_b32_e32 v125, 0xffff0000, v205
	v_mul_f32_e32 v114, 0xbfb8aa3b, v114
	v_mul_f32_e32 v115, 0xbfb8aa3b, v115
	v_exp_f32_e32 v100, v100
	v_exp_f32_e32 v101, v101
	v_pk_fma_f32 v[120:121], v[126:127], v[124:125], v[120:121]
	v_lshlrev_b32_e32 v124, 16, v203
	v_and_b32_e32 v125, 0xffff0000, v203
	v_add_f32_e32 v112, 1.0, v112
	v_add_f32_e32 v113, 1.0, v113
	v_exp_f32_e32 v114, v114
	v_exp_f32_e32 v115, v115
	v_mul_f32_e32 v110, 0xbfb8aa3b, v110
	v_mul_f32_e32 v111, 0xbfb8aa3b, v111
	v_pk_fma_f32 v[120:121], v[122:123], v[124:125], v[120:121]
	v_lshlrev_b32_e32 v122, 16, v201
	v_and_b32_e32 v123, 0xffff0000, v201
	v_readlane_b32 s38, v239, 33
	v_rcp_f32_e32 v112, v112
	v_rcp_f32_e32 v113, v113
	v_add_f32_e32 v108, 1.0, v108
	v_add_f32_e32 v109, 1.0, v109
	v_exp_f32_e32 v110, v110
	v_exp_f32_e32 v111, v111
	v_mul_f32_e32 v106, 0xbfb8aa3b, v106
	v_mul_f32_e32 v107, 0xbfb8aa3b, v107
	v_pk_fma_f32 v[118:119], v[118:119], v[122:123], v[120:121]
	v_readlane_b32 s39, v239, 34
	v_rcp_f32_e32 v108, v108
	v_rcp_f32_e32 v109, v109
	v_add_f32_e32 v104, 1.0, v104
	v_add_f32_e32 v105, 1.0, v105
	v_exp_f32_e32 v106, v106
	v_exp_f32_e32 v107, v107
	v_mul_f32_e32 v102, 0xbfb8aa3b, v102
	v_mul_f32_e32 v103, 0xbfb8aa3b, v103
	v_cvt_pk_bf16_f32 v116, v116, v117
	v_cvt_pk_bf16_f32 v117, v118, v119
	v_lshl_add_u64 v[118:119], s[38:39], 0, v[198:199]
	v_rcp_f32_e32 v104, v104
	v_rcp_f32_e32 v105, v105
	v_add_f32_e32 v100, 1.0, v100
	v_add_f32_e32 v101, 1.0, v101
	v_exp_f32_e32 v102, v102
	v_exp_f32_e32 v103, v103
	global_store_dwordx2 v[118:119], v[116:117], off sc1
	v_add_f32_e32 v114, 1.0, v114
	v_add_f32_e32 v115, 1.0, v115
	v_rcp_f32_e32 v100, v100
	v_rcp_f32_e32 v101, v101
	v_lshlrev_b32_e32 v116, 16, v196
	v_and_b32_e32 v117, 0xffff0000, v196
	v_rcp_f32_e32 v114, v114
	v_rcp_f32_e32 v115, v115
	v_add_f32_e32 v110, 1.0, v110
	v_add_f32_e32 v111, 1.0, v111
	v_pk_fma_f32 v[112:113], v[112:113], v[116:117], 0 op_sel_hi:[1,1,0]
	v_lshlrev_b32_e32 v116, 16, v194
	v_and_b32_e32 v117, 0xffff0000, v194
	v_rcp_f32_e32 v110, v110
	v_rcp_f32_e32 v111, v111
	v_add_f32_e32 v106, 1.0, v106
	v_add_f32_e32 v107, 1.0, v107
	v_pk_fma_f32 v[108:109], v[108:109], v[116:117], v[112:113]
	v_lshlrev_b32_e32 v112, 16, v192
	v_and_b32_e32 v113, 0xffff0000, v192
	v_mul_f32_e32 v96, 0xbfb8aa3b, v96
	v_mul_f32_e32 v97, 0xbfb8aa3b, v97
	v_rcp_f32_e32 v106, v106
	v_rcp_f32_e32 v107, v107
	v_pk_fma_f32 v[104:105], v[104:105], v[112:113], v[108:109]
	v_lshlrev_b32_e32 v108, 16, v190
	v_and_b32_e32 v109, 0xffff0000, v190
	v_add_f32_e32 v102, 1.0, v102
	v_add_f32_e32 v103, 1.0, v103
	v_exp_f32_e32 v96, v96
	v_exp_f32_e32 v97, v97
	v_mul_f32_e32 v92, 0xbfb8aa3b, v92
	v_mul_f32_e32 v93, 0xbfb8aa3b, v93
	v_pk_fma_f32 v[100:101], v[100:101], v[108:109], v[104:105]
	v_rcp_f32_e32 v102, v102
	v_rcp_f32_e32 v103, v103
	v_lshlrev_b32_e32 v104, 16, v197
	v_and_b32_e32 v105, 0xffff0000, v197
	v_exp_f32_e32 v92, v92
	v_exp_f32_e32 v93, v93
	v_mul_f32_e32 v88, 0xbfb8aa3b, v88
	v_mul_f32_e32 v89, 0xbfb8aa3b, v89
	v_pk_fma_f32 v[104:105], v[114:115], v[104:105], 0 op_sel_hi:[1,1,0]
	v_lshlrev_b32_e32 v108, 16, v195
	v_and_b32_e32 v109, 0xffff0000, v195
	v_exp_f32_e32 v88, v88
	v_exp_f32_e32 v89, v89
	v_mul_f32_e32 v84, 0xbfb8aa3b, v84
	v_mul_f32_e32 v85, 0xbfb8aa3b, v85
	v_pk_fma_f32 v[104:105], v[110:111], v[108:109], v[104:105]
	v_lshlrev_b32_e32 v108, 16, v193
	v_and_b32_e32 v109, 0xffff0000, v193
	v_mul_f32_e32 v98, 0xbfb8aa3b, v98
	v_mul_f32_e32 v99, 0xbfb8aa3b, v99
	v_exp_f32_e32 v84, v84
	v_exp_f32_e32 v85, v85
	v_pk_fma_f32 v[104:105], v[106:107], v[108:109], v[104:105]
	v_lshlrev_b32_e32 v106, 16, v191
	v_and_b32_e32 v107, 0xffff0000, v191
	v_add_f32_e32 v96, 1.0, v96
	v_add_f32_e32 v97, 1.0, v97
	v_exp_f32_e32 v98, v98
	v_exp_f32_e32 v99, v99
	v_mul_f32_e32 v94, 0xbfb8aa3b, v94
	v_mul_f32_e32 v95, 0xbfb8aa3b, v95
	v_pk_fma_f32 v[102:103], v[102:103], v[106:107], v[104:105]
	v_rcp_f32_e32 v96, v96
	v_rcp_f32_e32 v97, v97
	v_add_f32_e32 v92, 1.0, v92
	v_add_f32_e32 v93, 1.0, v93
	v_exp_f32_e32 v94, v94
	v_exp_f32_e32 v95, v95
	v_mul_f32_e32 v90, 0xbfb8aa3b, v90
	v_mul_f32_e32 v91, 0xbfb8aa3b, v91
	v_cvt_pk_bf16_f32 v100, v100, v101
	v_cvt_pk_bf16_f32 v101, v102, v103
	v_add_u32_e32 v102, 0x8000, v2
	v_mov_b32_e32 v103, v3
	v_rcp_f32_e32 v92, v92
	v_rcp_f32_e32 v93, v93
	v_add_f32_e32 v88, 1.0, v88
	v_add_f32_e32 v89, 1.0, v89
	v_exp_f32_e32 v90, v90
	v_exp_f32_e32 v91, v91
	v_mul_f32_e32 v86, 0xbfb8aa3b, v86
	v_mul_f32_e32 v87, 0xbfb8aa3b, v87
	v_lshl_add_u64 v[102:103], v[102:103], 1, s[38:39]
	v_rcp_f32_e32 v88, v88
	v_rcp_f32_e32 v89, v89
	v_add_f32_e32 v84, 1.0, v84
	v_add_f32_e32 v85, 1.0, v85
	v_exp_f32_e32 v86, v86
	v_exp_f32_e32 v87, v87
	global_store_dwordx2 v[102:103], v[100:101], off sc1
	v_add_f32_e32 v98, 1.0, v98
	v_add_f32_e32 v99, 1.0, v99
	v_rcp_f32_e32 v84, v84
	v_rcp_f32_e32 v85, v85
	v_lshlrev_b32_e32 v100, 16, v188
	v_and_b32_e32 v101, 0xffff0000, v188
	v_rcp_f32_e32 v98, v98
	v_rcp_f32_e32 v99, v99
	v_add_f32_e32 v94, 1.0, v94
	v_add_f32_e32 v95, 1.0, v95
	v_pk_fma_f32 v[96:97], v[96:97], v[100:101], 0 op_sel_hi:[1,1,0]
	v_lshlrev_b32_e32 v100, 16, v186
	v_and_b32_e32 v101, 0xffff0000, v186
	v_rcp_f32_e32 v94, v94
	v_rcp_f32_e32 v95, v95
	v_add_f32_e32 v90, 1.0, v90
	v_add_f32_e32 v91, 1.0, v91
	v_pk_fma_f32 v[92:93], v[92:93], v[100:101], v[96:97]
	v_lshlrev_b32_e32 v96, 16, v184
	v_and_b32_e32 v97, 0xffff0000, v184
	v_mul_f32_e32 v80, 0xbfb8aa3b, v80
	v_mul_f32_e32 v81, 0xbfb8aa3b, v81
	v_rcp_f32_e32 v90, v90
	v_rcp_f32_e32 v91, v91
	v_pk_fma_f32 v[88:89], v[88:89], v[96:97], v[92:93]
	v_lshlrev_b32_e32 v92, 16, v182
	v_and_b32_e32 v93, 0xffff0000, v182
	v_add_f32_e32 v86, 1.0, v86
	v_add_f32_e32 v87, 1.0, v87
	v_exp_f32_e32 v80, v80
	v_exp_f32_e32 v81, v81
	v_mul_f32_e32 v76, 0xbfb8aa3b, v76
	v_mul_f32_e32 v77, 0xbfb8aa3b, v77
	v_pk_fma_f32 v[84:85], v[84:85], v[92:93], v[88:89]
	v_rcp_f32_e32 v86, v86
	v_rcp_f32_e32 v87, v87
	v_lshlrev_b32_e32 v88, 16, v189
	v_and_b32_e32 v89, 0xffff0000, v189
	v_exp_f32_e32 v76, v76
	v_exp_f32_e32 v77, v77
	v_mul_f32_e32 v72, 0xbfb8aa3b, v72
	v_mul_f32_e32 v73, 0xbfb8aa3b, v73
	v_pk_fma_f32 v[88:89], v[98:99], v[88:89], 0 op_sel_hi:[1,1,0]
	v_lshlrev_b32_e32 v92, 16, v187
	v_and_b32_e32 v93, 0xffff0000, v187
	v_exp_f32_e32 v72, v72
	v_exp_f32_e32 v73, v73
	v_mul_f32_e32 v68, 0xbfb8aa3b, v68
	v_mul_f32_e32 v69, 0xbfb8aa3b, v69
	v_pk_fma_f32 v[88:89], v[94:95], v[92:93], v[88:89]
	v_lshlrev_b32_e32 v92, 16, v185
	v_and_b32_e32 v93, 0xffff0000, v185
	v_mul_f32_e32 v82, 0xbfb8aa3b, v82
	v_mul_f32_e32 v83, 0xbfb8aa3b, v83
	v_exp_f32_e32 v68, v68
	v_exp_f32_e32 v69, v69
	v_pk_fma_f32 v[88:89], v[90:91], v[92:93], v[88:89]
	v_lshlrev_b32_e32 v90, 16, v183
	v_and_b32_e32 v91, 0xffff0000, v183
	v_add_f32_e32 v80, 1.0, v80
	v_add_f32_e32 v81, 1.0, v81
	v_exp_f32_e32 v82, v82
	v_exp_f32_e32 v83, v83
	v_mul_f32_e32 v78, 0xbfb8aa3b, v78
	v_mul_f32_e32 v79, 0xbfb8aa3b, v79
	v_pk_fma_f32 v[86:87], v[86:87], v[90:91], v[88:89]
	v_rcp_f32_e32 v80, v80
	v_rcp_f32_e32 v81, v81
	v_add_f32_e32 v76, 1.0, v76
	v_add_f32_e32 v77, 1.0, v77
	v_exp_f32_e32 v78, v78
	v_exp_f32_e32 v79, v79
	v_mul_f32_e32 v74, 0xbfb8aa3b, v74
	v_mul_f32_e32 v75, 0xbfb8aa3b, v75
	v_cvt_pk_bf16_f32 v84, v84, v85
	v_cvt_pk_bf16_f32 v85, v86, v87
	v_add_u32_e32 v86, 0x10000, v2
	v_mov_b32_e32 v87, v3
	v_rcp_f32_e32 v76, v76
	v_rcp_f32_e32 v77, v77
	v_add_f32_e32 v72, 1.0, v72
	v_add_f32_e32 v73, 1.0, v73
	v_exp_f32_e32 v74, v74
	v_exp_f32_e32 v75, v75
	v_mul_f32_e32 v70, 0xbfb8aa3b, v70
	v_mul_f32_e32 v71, 0xbfb8aa3b, v71
	v_lshl_add_u64 v[86:87], v[86:87], 1, s[38:39]
	v_rcp_f32_e32 v72, v72
	v_rcp_f32_e32 v73, v73
	v_add_f32_e32 v68, 1.0, v68
	v_add_f32_e32 v69, 1.0, v69
	v_exp_f32_e32 v70, v70
	v_exp_f32_e32 v71, v71
	global_store_dwordx2 v[86:87], v[84:85], off sc1
	v_add_f32_e32 v82, 1.0, v82
	v_add_f32_e32 v83, 1.0, v83
	v_rcp_f32_e32 v68, v68
	v_rcp_f32_e32 v69, v69
	v_lshlrev_b32_e32 v84, 16, v180
	v_and_b32_e32 v85, 0xffff0000, v180
	v_rcp_f32_e32 v82, v82
	v_rcp_f32_e32 v83, v83
	v_add_f32_e32 v78, 1.0, v78
	v_add_f32_e32 v79, 1.0, v79
	v_pk_fma_f32 v[80:81], v[80:81], v[84:85], 0 op_sel_hi:[1,1,0]
	v_lshlrev_b32_e32 v84, 16, v178
	v_and_b32_e32 v85, 0xffff0000, v178
	v_rcp_f32_e32 v78, v78
	v_rcp_f32_e32 v79, v79
	v_add_f32_e32 v74, 1.0, v74
	v_add_f32_e32 v75, 1.0, v75
	v_pk_fma_f32 v[76:77], v[76:77], v[84:85], v[80:81]
	v_lshlrev_b32_e32 v80, 16, v176
	v_and_b32_e32 v81, 0xffff0000, v176
	v_rcp_f32_e32 v74, v74
	v_rcp_f32_e32 v75, v75
	v_pk_fma_f32 v[72:73], v[72:73], v[80:81], v[76:77]
	v_lshlrev_b32_e32 v76, 16, v174
	v_and_b32_e32 v77, 0xffff0000, v174
	v_add_f32_e32 v70, 1.0, v70
	v_add_f32_e32 v71, 1.0, v71
	v_pk_fma_f32 v[68:69], v[68:69], v[76:77], v[72:73]
	v_rcp_f32_e32 v70, v70
	v_rcp_f32_e32 v71, v71
	v_lshlrev_b32_e32 v72, 16, v181
	v_and_b32_e32 v73, 0xffff0000, v181
	v_pk_fma_f32 v[72:73], v[82:83], v[72:73], 0 op_sel_hi:[1,1,0]
	v_lshlrev_b32_e32 v76, 16, v179
	v_and_b32_e32 v77, 0xffff0000, v179
	v_pk_fma_f32 v[72:73], v[78:79], v[76:77], v[72:73]
	v_lshlrev_b32_e32 v76, 16, v177
	v_and_b32_e32 v77, 0xffff0000, v177
	v_pk_fma_f32 v[72:73], v[74:75], v[76:77], v[72:73]
	v_lshlrev_b32_e32 v74, 16, v175
	v_and_b32_e32 v75, 0xffff0000, v175
	v_pk_fma_f32 v[70:71], v[70:71], v[74:75], v[72:73]
	v_cvt_pk_bf16_f32 v68, v68, v69
	v_cvt_pk_bf16_f32 v69, v70, v71
	v_add_u32_e32 v70, 0x18000, v2
	v_mov_b32_e32 v71, v3
	v_lshl_add_u64 v[70:71], v[70:71], 1, s[38:39]
	v_mul_f32_e32 v64, 0xbfb8aa3b, v64
	global_store_dwordx2 v[70:71], v[68:69], off sc1
	v_exp_f32_e32 v68, v64
	v_mul_f32_e32 v64, 0xbfb8aa3b, v65
	v_exp_f32_e32 v65, v64
	v_mul_f32_e32 v60, 0xbfb8aa3b, v60
	v_mul_f32_e32 v61, 0xbfb8aa3b, v61
	v_exp_f32_e32 v60, v60
	v_exp_f32_e32 v61, v61
	v_mul_f32_e32 v56, 0xbfb8aa3b, v56
	v_mul_f32_e32 v57, 0xbfb8aa3b, v57
	v_mul_f32_e32 v66, 0xbfb8aa3b, v66
	v_exp_f32_e32 v56, v56
	v_exp_f32_e32 v57, v57
	v_mul_f32_e32 v52, 0xbfb8aa3b, v52
	v_mul_f32_e32 v53, 0xbfb8aa3b, v53
	v_exp_f32_e32 v66, v66
	v_mul_f32_e32 v67, 0xbfb8aa3b, v67
	v_exp_f32_e32 v52, v52
	v_exp_f32_e32 v53, v53
	v_add_f32_e32 v68, 1.0, v68
	v_add_f32_e32 v65, 1.0, v65
	v_exp_f32_e32 v67, v67
	v_mul_f32_e32 v62, 0xbfb8aa3b, v62
	v_mul_f32_e32 v63, 0xbfb8aa3b, v63
	v_rcp_f32_e32 v68, v68
	v_rcp_f32_e32 v69, v65
	v_add_f32_e32 v60, 1.0, v60
	v_add_f32_e32 v61, 1.0, v61
	v_exp_f32_e32 v62, v62
	v_exp_f32_e32 v63, v63
	v_mul_f32_e32 v58, 0xbfb8aa3b, v58
	v_mul_f32_e32 v59, 0xbfb8aa3b, v59
	v_rcp_f32_e32 v60, v60
	v_rcp_f32_e32 v61, v61
	v_add_f32_e32 v56, 1.0, v56
	v_add_f32_e32 v57, 1.0, v57
	v_exp_f32_e32 v58, v58
	v_exp_f32_e32 v59, v59
	v_mul_f32_e32 v54, 0xbfb8aa3b, v54
	v_mul_f32_e32 v55, 0xbfb8aa3b, v55
	v_add_f32_e32 v65, 1.0, v66
	v_rcp_f32_e32 v56, v56
	v_rcp_f32_e32 v57, v57
	v_add_f32_e32 v52, 1.0, v52
	v_add_f32_e32 v53, 1.0, v53
	v_exp_f32_e32 v54, v54
	v_exp_f32_e32 v55, v55
	v_rcp_f32_e32 v66, v65
	v_add_f32_e32 v65, 1.0, v67
	v_rcp_f32_e32 v52, v52
	v_rcp_f32_e32 v53, v53
	v_lshlrev_b32_e32 v70, 16, v172
	v_and_b32_e32 v71, 0xffff0000, v172
	v_rcp_f32_e32 v67, v65
	v_add_f32_e32 v62, 1.0, v62
	v_add_f32_e32 v63, 1.0, v63
	v_pk_fma_f32 v[68:69], v[68:69], v[70:71], 0 op_sel_hi:[1,1,0]
	v_lshlrev_b32_e32 v70, 16, v170
	v_and_b32_e32 v71, 0xffff0000, v170
	v_mul_f32_e32 v48, 0xbfb8aa3b, v48
	v_mul_f32_e32 v49, 0xbfb8aa3b, v49
	v_rcp_f32_e32 v62, v62
	v_rcp_f32_e32 v63, v63
	v_add_f32_e32 v58, 1.0, v58
	v_add_f32_e32 v59, 1.0, v59
	v_pk_fma_f32 v[60:61], v[60:61], v[70:71], v[68:69]
	v_lshlrev_b32_e32 v68, 16, v168
	v_and_b32_e32 v69, 0xffff0000, v168
	v_exp_f32_e32 v48, v48
	v_exp_f32_e32 v49, v49
	v_mul_f32_e32 v44, 0xbfb8aa3b, v44
	v_mul_f32_e32 v45, 0xbfb8aa3b, v45
	v_rcp_f32_e32 v58, v58
	v_rcp_f32_e32 v59, v59
	v_pk_fma_f32 v[56:57], v[56:57], v[68:69], v[60:61]
	v_lshlrev_b32_e32 v60, 16, v166
	v_and_b32_e32 v61, 0xffff0000, v166
	v_add_f32_e32 v54, 1.0, v54
	v_add_f32_e32 v55, 1.0, v55
	v_exp_f32_e32 v44, v44
	v_exp_f32_e32 v45, v45
	v_mul_f32_e32 v40, 0xbfb8aa3b, v40
	v_mul_f32_e32 v41, 0xbfb8aa3b, v41
	v_pk_fma_f32 v[52:53], v[52:53], v[60:61], v[56:57]
	v_rcp_f32_e32 v54, v54
	v_rcp_f32_e32 v55, v55
	v_lshlrev_b32_e32 v56, 16, v173
	v_and_b32_e32 v57, 0xffff0000, v173
	v_exp_f32_e32 v40, v40
	v_exp_f32_e32 v41, v41
	v_mul_f32_e32 v36, 0xbfb8aa3b, v36
	v_mul_f32_e32 v37, 0xbfb8aa3b, v37
	v_pk_fma_f32 v[56:57], v[66:67], v[56:57], 0 op_sel_hi:[1,1,0]
	v_lshlrev_b32_e32 v60, 16, v171
	v_and_b32_e32 v61, 0xffff0000, v171
	v_mul_f32_e32 v50, 0xbfb8aa3b, v50
	v_mul_f32_e32 v51, 0xbfb8aa3b, v51
	v_exp_f32_e32 v36, v36
	v_exp_f32_e32 v37, v37
	v_pk_fma_f32 v[56:57], v[62:63], v[60:61], v[56:57]
	v_lshlrev_b32_e32 v60, 16, v169
	v_and_b32_e32 v61, 0xffff0000, v169
	v_add_f32_e32 v48, 1.0, v48
	v_add_f32_e32 v49, 1.0, v49
	v_exp_f32_e32 v50, v50
	v_exp_f32_e32 v51, v51
	v_mul_f32_e32 v46, 0xbfb8aa3b, v46
	v_mul_f32_e32 v47, 0xbfb8aa3b, v47
	v_pk_fma_f32 v[56:57], v[58:59], v[60:61], v[56:57]
	v_lshlrev_b32_e32 v58, 16, v167
	v_and_b32_e32 v59, 0xffff0000, v167
	v_rcp_f32_e32 v48, v48
	v_rcp_f32_e32 v49, v49
	v_add_f32_e32 v44, 1.0, v44
	v_add_f32_e32 v45, 1.0, v45
	v_exp_f32_e32 v46, v46
	v_exp_f32_e32 v47, v47
	v_mul_f32_e32 v42, 0xbfb8aa3b, v42
	v_mul_f32_e32 v43, 0xbfb8aa3b, v43
	v_add_u32_e32 v64, 0x40000, v2
	v_pk_fma_f32 v[54:55], v[54:55], v[58:59], v[56:57]
	v_mov_b32_e32 v65, v3
	v_rcp_f32_e32 v44, v44
	v_rcp_f32_e32 v45, v45
	v_add_f32_e32 v40, 1.0, v40
	v_add_f32_e32 v41, 1.0, v41
	v_exp_f32_e32 v42, v42
	v_exp_f32_e32 v43, v43
	v_mul_f32_e32 v38, 0xbfb8aa3b, v38
	v_mul_f32_e32 v39, 0xbfb8aa3b, v39
	v_cvt_pk_bf16_f32 v52, v52, v53
	v_cvt_pk_bf16_f32 v53, v54, v55
	v_lshl_add_u64 v[54:55], v[64:65], 1, s[38:39]
	v_rcp_f32_e32 v40, v40
	v_rcp_f32_e32 v41, v41
	v_add_f32_e32 v36, 1.0, v36
	v_add_f32_e32 v37, 1.0, v37
	v_exp_f32_e32 v38, v38
	v_exp_f32_e32 v39, v39
	global_store_dwordx2 v[54:55], v[52:53], off sc1
	v_add_f32_e32 v50, 1.0, v50
	v_add_f32_e32 v51, 1.0, v51
	v_rcp_f32_e32 v36, v36
	v_rcp_f32_e32 v37, v37
	v_lshlrev_b32_e32 v52, 16, v164
	v_and_b32_e32 v53, 0xffff0000, v164
	v_rcp_f32_e32 v50, v50
	v_rcp_f32_e32 v51, v51
	v_add_f32_e32 v46, 1.0, v46
	v_add_f32_e32 v47, 1.0, v47
	v_pk_fma_f32 v[48:49], v[48:49], v[52:53], 0 op_sel_hi:[1,1,0]
	v_lshlrev_b32_e32 v52, 16, v162
	v_and_b32_e32 v53, 0xffff0000, v162
	v_rcp_f32_e32 v46, v46
	v_rcp_f32_e32 v47, v47
	v_add_f32_e32 v42, 1.0, v42
	v_add_f32_e32 v43, 1.0, v43
	v_pk_fma_f32 v[44:45], v[44:45], v[52:53], v[48:49]
	v_lshlrev_b32_e32 v48, 16, v160
	v_and_b32_e32 v49, 0xffff0000, v160
	v_mul_f32_e32 v32, 0xbfb8aa3b, v32
	v_mul_f32_e32 v33, 0xbfb8aa3b, v33
	v_rcp_f32_e32 v42, v42
	v_rcp_f32_e32 v43, v43
	v_pk_fma_f32 v[40:41], v[40:41], v[48:49], v[44:45]
	v_lshlrev_b32_e32 v44, 16, v158
	v_and_b32_e32 v45, 0xffff0000, v158
	v_add_f32_e32 v38, 1.0, v38
	v_add_f32_e32 v39, 1.0, v39
	v_exp_f32_e32 v32, v32
	v_exp_f32_e32 v33, v33
	v_mul_f32_e32 v28, 0xbfb8aa3b, v28
	v_mul_f32_e32 v29, 0xbfb8aa3b, v29
	v_pk_fma_f32 v[36:37], v[36:37], v[44:45], v[40:41]
	v_rcp_f32_e32 v38, v38
	v_rcp_f32_e32 v39, v39
	v_lshlrev_b32_e32 v40, 16, v165
	v_and_b32_e32 v41, 0xffff0000, v165
	v_exp_f32_e32 v28, v28
	v_exp_f32_e32 v29, v29
	v_mul_f32_e32 v24, 0xbfb8aa3b, v24
	v_mul_f32_e32 v25, 0xbfb8aa3b, v25
	v_pk_fma_f32 v[40:41], v[50:51], v[40:41], 0 op_sel_hi:[1,1,0]
	v_lshlrev_b32_e32 v44, 16, v163
	v_and_b32_e32 v45, 0xffff0000, v163
	v_exp_f32_e32 v24, v24
	v_exp_f32_e32 v25, v25
	v_mul_f32_e32 v20, 0xbfb8aa3b, v20
	v_mul_f32_e32 v21, 0xbfb8aa3b, v21
	v_pk_fma_f32 v[40:41], v[46:47], v[44:45], v[40:41]
	v_lshlrev_b32_e32 v44, 16, v161
	v_and_b32_e32 v45, 0xffff0000, v161
	v_mul_f32_e32 v34, 0xbfb8aa3b, v34
	v_mul_f32_e32 v35, 0xbfb8aa3b, v35
	v_exp_f32_e32 v20, v20
	v_exp_f32_e32 v21, v21
	v_pk_fma_f32 v[40:41], v[42:43], v[44:45], v[40:41]
	v_lshlrev_b32_e32 v42, 16, v159
	v_and_b32_e32 v43, 0xffff0000, v159
	v_add_f32_e32 v32, 1.0, v32
	v_add_f32_e32 v33, 1.0, v33
	v_exp_f32_e32 v34, v34
	v_exp_f32_e32 v35, v35
	v_mul_f32_e32 v30, 0xbfb8aa3b, v30
	v_mul_f32_e32 v31, 0xbfb8aa3b, v31
	v_pk_fma_f32 v[38:39], v[38:39], v[42:43], v[40:41]
	v_rcp_f32_e32 v32, v32
	v_rcp_f32_e32 v33, v33
	v_add_f32_e32 v28, 1.0, v28
	v_add_f32_e32 v29, 1.0, v29
	v_exp_f32_e32 v30, v30
	v_exp_f32_e32 v31, v31
	v_mul_f32_e32 v26, 0xbfb8aa3b, v26
	v_mul_f32_e32 v27, 0xbfb8aa3b, v27
	v_cvt_pk_bf16_f32 v36, v36, v37
	v_cvt_pk_bf16_f32 v37, v38, v39
	v_add_u32_e32 v38, 0x48000, v2
	v_mov_b32_e32 v39, v3
	v_rcp_f32_e32 v28, v28
	v_rcp_f32_e32 v29, v29
	v_add_f32_e32 v24, 1.0, v24
	v_add_f32_e32 v25, 1.0, v25
	v_exp_f32_e32 v26, v26
	v_exp_f32_e32 v27, v27
	v_mul_f32_e32 v22, 0xbfb8aa3b, v22
	v_mul_f32_e32 v23, 0xbfb8aa3b, v23
	v_lshl_add_u64 v[38:39], v[38:39], 1, s[38:39]
	v_rcp_f32_e32 v24, v24
	v_rcp_f32_e32 v25, v25
	v_add_f32_e32 v20, 1.0, v20
	v_add_f32_e32 v21, 1.0, v21
	v_exp_f32_e32 v22, v22
	v_exp_f32_e32 v23, v23
	global_store_dwordx2 v[38:39], v[36:37], off sc1
	v_add_f32_e32 v34, 1.0, v34
	v_add_f32_e32 v35, 1.0, v35
	v_rcp_f32_e32 v20, v20
	v_rcp_f32_e32 v21, v21
	v_lshlrev_b32_e32 v36, 16, v156
	v_and_b32_e32 v37, 0xffff0000, v156
	v_rcp_f32_e32 v34, v34
	v_rcp_f32_e32 v35, v35
	v_add_f32_e32 v30, 1.0, v30
	v_add_f32_e32 v31, 1.0, v31
	v_pk_fma_f32 v[32:33], v[32:33], v[36:37], 0 op_sel_hi:[1,1,0]
	v_lshlrev_b32_e32 v36, 16, v154
	v_and_b32_e32 v37, 0xffff0000, v154
	v_rcp_f32_e32 v30, v30
	v_rcp_f32_e32 v31, v31
	v_add_f32_e32 v26, 1.0, v26
	v_add_f32_e32 v27, 1.0, v27
	v_pk_fma_f32 v[28:29], v[28:29], v[36:37], v[32:33]
	v_lshlrev_b32_e32 v32, 16, v152
	v_and_b32_e32 v33, 0xffff0000, v152
	v_mul_f32_e32 v16, 0xbfb8aa3b, v16
	v_mul_f32_e32 v17, 0xbfb8aa3b, v17
	v_rcp_f32_e32 v26, v26
	v_rcp_f32_e32 v27, v27
	v_pk_fma_f32 v[24:25], v[24:25], v[32:33], v[28:29]
	v_lshlrev_b32_e32 v28, 16, v150
	v_and_b32_e32 v29, 0xffff0000, v150
	v_add_f32_e32 v22, 1.0, v22
	v_add_f32_e32 v23, 1.0, v23
	v_exp_f32_e32 v16, v16
	v_exp_f32_e32 v17, v17
	v_mul_f32_e32 v12, 0xbfb8aa3b, v12
	v_mul_f32_e32 v13, 0xbfb8aa3b, v13
	v_pk_fma_f32 v[20:21], v[20:21], v[28:29], v[24:25]
	v_rcp_f32_e32 v22, v22
	v_rcp_f32_e32 v23, v23
	v_lshlrev_b32_e32 v24, 16, v157
	v_and_b32_e32 v25, 0xffff0000, v157
	v_exp_f32_e32 v12, v12
	v_exp_f32_e32 v13, v13
	v_mul_f32_e32 v8, 0xbfb8aa3b, v8
	v_mul_f32_e32 v9, 0xbfb8aa3b, v9
	v_pk_fma_f32 v[24:25], v[34:35], v[24:25], 0 op_sel_hi:[1,1,0]
	v_lshlrev_b32_e32 v28, 16, v155
	v_and_b32_e32 v29, 0xffff0000, v155
	v_exp_f32_e32 v8, v8
	v_exp_f32_e32 v9, v9
	v_mul_f32_e32 v4, 0xbfb8aa3b, v4
	v_mul_f32_e32 v5, 0xbfb8aa3b, v5
	v_pk_fma_f32 v[24:25], v[30:31], v[28:29], v[24:25]
	v_lshlrev_b32_e32 v28, 16, v153
	v_and_b32_e32 v29, 0xffff0000, v153
	v_mul_f32_e32 v18, 0xbfb8aa3b, v18
	v_mul_f32_e32 v19, 0xbfb8aa3b, v19
	v_exp_f32_e32 v4, v4
	v_exp_f32_e32 v5, v5
	v_pk_fma_f32 v[24:25], v[26:27], v[28:29], v[24:25]
	v_lshlrev_b32_e32 v26, 16, v151
	v_and_b32_e32 v27, 0xffff0000, v151
	v_add_f32_e32 v16, 1.0, v16
	v_add_f32_e32 v17, 1.0, v17
	v_exp_f32_e32 v18, v18
	v_exp_f32_e32 v19, v19
	v_mul_f32_e32 v14, 0xbfb8aa3b, v14
	v_mul_f32_e32 v15, 0xbfb8aa3b, v15
	v_pk_fma_f32 v[22:23], v[22:23], v[26:27], v[24:25]
	v_rcp_f32_e32 v16, v16
	v_rcp_f32_e32 v17, v17
	v_add_f32_e32 v12, 1.0, v12
	v_add_f32_e32 v13, 1.0, v13
	v_exp_f32_e32 v14, v14
	v_exp_f32_e32 v15, v15
	v_mul_f32_e32 v10, 0xbfb8aa3b, v10
	v_mul_f32_e32 v11, 0xbfb8aa3b, v11
	v_cvt_pk_bf16_f32 v20, v20, v21
	v_cvt_pk_bf16_f32 v21, v22, v23
	v_add_u32_e32 v22, 0x50000, v2
	v_mov_b32_e32 v23, v3
	v_rcp_f32_e32 v12, v12
	v_rcp_f32_e32 v13, v13
	v_add_f32_e32 v8, 1.0, v8
	v_add_f32_e32 v9, 1.0, v9
	v_exp_f32_e32 v10, v10
	v_exp_f32_e32 v11, v11
	v_mul_f32_e32 v6, 0xbfb8aa3b, v6
	v_mul_f32_e32 v7, 0xbfb8aa3b, v7
	v_lshl_add_u64 v[22:23], v[22:23], 1, s[38:39]
	v_rcp_f32_e32 v8, v8
	v_rcp_f32_e32 v9, v9
	v_add_f32_e32 v4, 1.0, v4
	v_add_f32_e32 v5, 1.0, v5
	v_exp_f32_e32 v6, v6
	v_exp_f32_e32 v7, v7
	global_store_dwordx2 v[22:23], v[20:21], off sc1
	v_add_f32_e32 v18, 1.0, v18
	v_add_f32_e32 v19, 1.0, v19
	v_rcp_f32_e32 v4, v4
	v_rcp_f32_e32 v5, v5
	v_lshlrev_b32_e32 v20, 16, v148
	v_and_b32_e32 v21, 0xffff0000, v148
	v_rcp_f32_e32 v18, v18
	v_rcp_f32_e32 v19, v19
	v_add_f32_e32 v14, 1.0, v14
	v_add_f32_e32 v15, 1.0, v15
	v_pk_fma_f32 v[16:17], v[16:17], v[20:21], 0 op_sel_hi:[1,1,0]
	v_lshlrev_b32_e32 v20, 16, v146
	v_and_b32_e32 v21, 0xffff0000, v146
	v_rcp_f32_e32 v14, v14
	v_rcp_f32_e32 v15, v15
	v_add_f32_e32 v10, 1.0, v10
	v_add_f32_e32 v11, 1.0, v11
	v_pk_fma_f32 v[12:13], v[12:13], v[20:21], v[16:17]
	v_lshlrev_b32_e32 v16, 16, v144
	v_and_b32_e32 v17, 0xffff0000, v144
	v_rcp_f32_e32 v10, v10
	v_rcp_f32_e32 v11, v11
	v_pk_fma_f32 v[8:9], v[8:9], v[16:17], v[12:13]
	v_lshlrev_b32_e32 v12, 16, v128
	v_and_b32_e32 v13, 0xffff0000, v128
	v_add_f32_e32 v6, 1.0, v6
	v_add_f32_e32 v7, 1.0, v7
	v_pk_fma_f32 v[4:5], v[4:5], v[12:13], v[8:9]
	v_rcp_f32_e32 v6, v6
	v_rcp_f32_e32 v7, v7
	v_lshlrev_b32_e32 v8, 16, v149
	v_and_b32_e32 v9, 0xffff0000, v149
	v_pk_fma_f32 v[8:9], v[18:19], v[8:9], 0 op_sel_hi:[1,1,0]
	v_lshlrev_b32_e32 v12, 16, v147
	v_and_b32_e32 v13, 0xffff0000, v147
	v_pk_fma_f32 v[8:9], v[14:15], v[12:13], v[8:9]
	v_lshlrev_b32_e32 v12, 16, v145
	v_and_b32_e32 v13, 0xffff0000, v145
	v_pk_fma_f32 v[8:9], v[10:11], v[12:13], v[8:9]
	v_lshlrev_b32_e32 v10, 16, v129
	v_and_b32_e32 v11, 0xffff0000, v129
	v_pk_fma_f32 v[6:7], v[6:7], v[10:11], v[8:9]
	v_add_u32_e32 v2, 0x58000, v2
	v_readlane_b32 s88, v239, 24
	v_cvt_pk_bf16_f32 v4, v4, v5
	v_cvt_pk_bf16_f32 v5, v6, v7
	v_lshl_add_u64 v[6:7], v[2:3], 1, s[38:39]
	s_andn2_b64 vcc, exec, s[6:7]
	s_mov_b64 s[6:7], -1
	v_readlane_b32 s89, v239, 25
	v_readlane_b32 s90, v239, 26
	v_readlane_b32 s91, v239, 27
	global_store_dwordx2 v[6:7], v[4:5], off sc1
	s_cbranch_vccnz .LBB0_724
	s_andn2_b64 vcc, exec, s[0:1]
	s_cbranch_vccnz .LBB0_723
	s_barrier
	s_branch .LBB0_723

.LBB0_808:
	v_lshl_add_u32 v146, s83, 8, v1
	s_lshl_b32 s38, s82, 8
	s_ashr_i32 s39, s38, 31
	v_ashrrev_i32_e32 v147, 31, v146
	v_lshl_add_u64 v[148:149], s[38:39], 1, v[138:139]
	v_lshlrev_b64 v[150:151], 12, v[146:147]
	v_lshl_add_u64 v[150:151], v[148:149], 0, v[150:151]
	s_mov_b32 s9, 0x80000
	s_mov_b64 s[38:39], 0x80000
	v_cvt_pk_bf16_f32 v64, v64, v65
	v_cvt_pk_bf16_f32 v65, v66, v67
	v_cvt_pk_bf16_f32 v66, v60, v61
	v_add_co_u32_e32 v60, vcc, s9, v150
	v_cvt_pk_bf16_f32 v72, v72, v73
	v_cvt_pk_bf16_f32 v73, v74, v75
	v_cvt_pk_bf16_f32 v74, v68, v69
	v_lshl_add_u64 v[68:69], v[150:151], 0, s[38:39]
	v_addc_co_u32_e32 v61, vcc, 0, v151, vcc
	v_cvt_pk_bf16_f32 v48, v48, v49
	v_cvt_pk_bf16_f32 v49, v50, v51
	v_cvt_pk_bf16_f32 v50, v44, v45
	v_cvt_pk_bf16_f32 v51, v46, v47
	s_mov_b32 s9, 0x90000
	global_store_dwordx4 v[68:69], v[48:51], off offset:256 sc1
	s_mov_b64 s[38:39], 0x90000
	v_cvt_pk_bf16_f32 v112, v112, v113
	v_add_co_u32_e32 v50, vcc, s9, v150
	v_cvt_pk_bf16_f32 v113, v114, v115
	v_cvt_pk_bf16_f32 v114, v108, v109
	v_or_b32_e32 v108, 16, v146
	v_lshl_add_u64 v[48:49], v[150:151], 0, s[38:39]
	v_addc_co_u32_e32 v51, vcc, 0, v151, vcc
	v_cvt_pk_bf16_f32 v32, v32, v33
	v_cvt_pk_bf16_f32 v33, v34, v35
	v_cvt_pk_bf16_f32 v34, v28, v29
	v_cvt_pk_bf16_f32 v35, v30, v31
	s_mov_b32 s9, 0xa0000
	v_ashrrev_i32_e32 v109, 31, v108
	v_cvt_pk_bf16_f32 v96, v96, v97
	v_cvt_pk_bf16_f32 v97, v98, v99
	v_cvt_pk_bf16_f32 v98, v92, v93
	v_or_b32_e32 v92, 32, v146
	global_store_dwordx4 v[48:49], v[32:35], off offset:256 sc1
	s_mov_b64 s[38:39], 0xa0000
	v_cvt_pk_bf16_f32 v115, v110, v111
	v_add_co_u32_e32 v34, vcc, s9, v150
	v_lshlrev_b64 v[108:109], 12, v[108:109]
	v_ashrrev_i32_e32 v93, 31, v92
	v_cvt_pk_bf16_f32 v80, v80, v81
	v_cvt_pk_bf16_f32 v81, v82, v83
	v_cvt_pk_bf16_f32 v82, v76, v77
	v_or_b32_e32 v76, 48, v146
	v_lshl_add_u64 v[32:33], v[150:151], 0, s[38:39]
	v_addc_co_u32_e32 v35, vcc, 0, v151, vcc
	v_cvt_pk_bf16_f32 v16, v16, v17
	v_cvt_pk_bf16_f32 v17, v18, v19
	v_cvt_pk_bf16_f32 v18, v12, v13
	v_cvt_pk_bf16_f32 v19, v14, v15
	s_mov_b32 s9, 0xb0000
	global_store_dwordx4 v[150:151], v[112:115], off offset:256 sc1
	v_cvt_pk_bf16_f32 v99, v94, v95
	v_lshlrev_b64 v[92:93], 12, v[92:93]
	v_lshl_add_u64 v[112:113], v[148:149], 0, v[108:109]
	v_ashrrev_i32_e32 v77, 31, v76
	global_store_dwordx4 v[32:33], v[16:19], off offset:256 sc1
	global_store_dwordx4 v[112:113], v[96:99], off offset:256 sc1
	v_cvt_pk_bf16_f32 v83, v78, v79
	v_add_co_u32_e32 v18, vcc, s9, v150
	v_lshl_add_u64 v[96:97], v[148:149], 0, v[92:93]
	v_lshlrev_b64 v[76:77], 12, v[76:77]
	s_mov_b64 s[38:39], 0xb0000
	v_addc_co_u32_e32 v19, vcc, 0, v151, vcc
	v_readlane_b32 s88, v239, 24
	v_cvt_pk_bf16_f32 v128, v128, v129
	v_cvt_pk_bf16_f32 v129, v130, v131
	v_cvt_pk_bf16_f32 v130, v124, v125
	v_cvt_pk_bf16_f32 v131, v126, v127
	v_cvt_pk_bf16_f32 v108, v120, v121
	v_cvt_pk_bf16_f32 v109, v122, v123
	v_cvt_pk_bf16_f32 v110, v116, v117
	v_cvt_pk_bf16_f32 v111, v118, v119
	v_cvt_pk_bf16_f32 v92, v104, v105
	v_cvt_pk_bf16_f32 v93, v106, v107
	v_cvt_pk_bf16_f32 v94, v100, v101
	v_cvt_pk_bf16_f32 v95, v102, v103
	global_store_dwordx4 v[96:97], v[80:83], off offset:256 sc1
	v_cvt_pk_bf16_f32 v78, v84, v85
	v_cvt_pk_bf16_f32 v79, v86, v87
	v_lshl_add_u64 v[80:81], v[148:149], 0, v[76:77]
	v_cvt_pk_bf16_f32 v76, v88, v89
	v_cvt_pk_bf16_f32 v77, v90, v91
	v_cvt_pk_bf16_f32 v75, v70, v71
	v_cvt_pk_bf16_f32 v67, v62, v63
	v_cvt_pk_bf16_f32 v44, v56, v57
	v_cvt_pk_bf16_f32 v45, v58, v59
	v_cvt_pk_bf16_f32 v46, v52, v53
	v_cvt_pk_bf16_f32 v47, v54, v55
	v_cvt_pk_bf16_f32 v28, v40, v41
	v_cvt_pk_bf16_f32 v29, v42, v43
	v_cvt_pk_bf16_f32 v30, v36, v37
	v_cvt_pk_bf16_f32 v31, v38, v39
	v_lshl_add_u64 v[16:17], v[150:151], 0, s[38:39]
	v_cvt_pk_bf16_f32 v12, v24, v25
	v_cvt_pk_bf16_f32 v13, v26, v27
	v_cvt_pk_bf16_f32 v14, v20, v21
	v_cvt_pk_bf16_f32 v15, v22, v23
	v_cvt_pk_bf16_f32 v8, v8, v9
	v_cvt_pk_bf16_f32 v9, v10, v11
	v_cvt_pk_bf16_f32 v10, v4, v5
	v_cvt_pk_bf16_f32 v11, v6, v7
	s_andn2_b64 vcc, exec, s[6:7]
	s_mov_b64 s[6:7], -1
	v_readlane_b32 s89, v239, 25
	v_readlane_b32 s90, v239, 26
	v_readlane_b32 s91, v239, 27
	global_store_dwordx4 v[150:151], v[128:131], off sc1
	global_store_dwordx4 v[112:113], v[108:111], off sc1
	global_store_dwordx4 v[96:97], v[92:95], off sc1
	global_store_dwordx4 v[80:81], v[76:79], off sc1
	global_store_dwordx4 v[80:81], v[72:75], off offset:256 sc1
	global_store_dwordx4 v[60:61], v[64:67], off sc1
	global_store_dwordx4 v[50:51], v[44:47], off sc1
	global_store_dwordx4 v[34:35], v[28:31], off sc1
	global_store_dwordx4 v[18:19], v[12:15], off sc1
	global_store_dwordx4 v[16:17], v[8:11], off offset:256 sc1
	s_cbranch_vccnz .LBB0_797
	s_andn2_b64 vcc, exec, s[0:1]
	s_cbranch_vccnz .LBB0_796
	s_barrier
	s_branch .LBB0_796
